# q6 + phase-A converter budget 4.5 grabs instead of 5
# baseline (speedup 1.0000x reference)
.LBB0_181:
	s_mul_i32 s6, s90, 0xd760
	s_max_i32 s57, s50, s6
	s_sub_i32 s86, s25, s92
	s_and_b64 s[6:7], s[2:3], exec
	s_movk_i32 s4, 0x80
	s_cselect_b32 s6, s4, 0x120
	s_mul_i32 s6, s6, s86
	s_add_i32 s6, s6, s57
	s_min_i32 s50, s6, 0x34920
	s_cmp_lt_i32 s89, 0
	s_mov_b64 s[6:7], -1
	s_cbranch_scc0 .LBB0_712
	s_andn2_b64 vcc, exec, s[2:3]
	s_not_b32 s68, s89
	s_cbranch_vccnz .LBB0_260
	s_add_u32 s26, s52, 0x37200000
	s_addc_u32 s27, s53, 0
	s_add_u32 s28, s52, 0x5200000
	s_addc_u32 s29, s53, 0
	s_waitcnt vmcnt(0)
	v_mov_b32_e32 v1, v0
	s_cmp_gt_u32 s89, 0xffffffdf
	s_cselect_b64 s[6:7], -1, 0
	s_cmp_lt_u32 s89, 0xffffffe0
	v_readfirstlane_b32 s3, v1
	s_cbranch_scc1 .LBB0_185
	s_lshr_b32 s8, s68, 3
	s_and_b32 s2, s68, 7
	s_lshl_b32 s9, s8, 20
	s_add_u32 s18, s26, s9
	s_addc_u32 s19, s27, 0
	s_lshl_b32 s9, s2, 20
	s_add_u32 s20, s28, s9
	s_addc_u32 s21, s29, 0
	s_lshl_b32 s30, s8, 8
	s_lshl_b32 s2, s2, 8
